# MoE table set-up (P9/P10/P11 prologues): the 32 expert-count loads issued together instead of 32 dependent load-wait round trips
# baseline (speedup 1.0000x reference)
; #define LAS __attribute__((address_space(3)))
; __device__ __forceinline__ void moe_tables(Frame& F) {
;     LAS int* tab = (LAS int*)(F.lds + TAB_OFF);
;     if (F.tid == 0) { int run = 0;
;         for (int e = 0; e < NE; ++e) { const int c = (int)__hip_atomic_load(F.ctl + CW_CNT + e, RLX_AGENT); const int p = (c + 255) / 256 * 256; tab[32 + e] = run; run += p; tab[e] = run; }
;         tab[64] = run / 256; }
;     __syncthreads();
; }
.LBB0_1573:
	s_or_b64 exec, exec, s[0:1]
	s_waitcnt vmcnt(15)
	v_mov_b32_e32 v2, v0
	s_waitcnt lgkmcnt(0)
	s_barrier
	s_nop 0
	v_readfirstlane_b32 s10, v2
	v_cmp_eq_u32_e32 vcc, 0, v2
	s_and_saveexec_b64 s[0:1], vcc
	s_cbranch_execz .LBB0_1575
	v_mov_b32_e32 v1, 0
	global_load_dword v3, v1, s[96:97] offset:2048 sc1
	global_load_dword v16, v1, s[96:97] offset:2052 sc1
	global_load_dword v17, v1, s[96:97] offset:2056 sc1
	global_load_dword v18, v1, s[96:97] offset:2060 sc1
	global_load_dword v19, v1, s[96:97] offset:2064 sc1
	global_load_dword v20, v1, s[96:97] offset:2068 sc1
	global_load_dword v21, v1, s[96:97] offset:2072 sc1
	global_load_dword v22, v1, s[96:97] offset:2076 sc1
	global_load_dword v23, v1, s[96:97] offset:2080 sc1
	global_load_dword v24, v1, s[96:97] offset:2084 sc1
	global_load_dword v25, v1, s[96:97] offset:2088 sc1
	global_load_dword v26, v1, s[96:97] offset:2092 sc1
	global_load_dword v27, v1, s[96:97] offset:2096 sc1
	global_load_dword v28, v1, s[96:97] offset:2100 sc1
	global_load_dword v29, v1, s[96:97] offset:2104 sc1
	global_load_dword v30, v1, s[96:97] offset:2108 sc1
	global_load_dword v31, v1, s[96:97] offset:2112 sc1
	global_load_dword v32, v1, s[96:97] offset:2116 sc1
	global_load_dword v33, v1, s[96:97] offset:2120 sc1
	global_load_dword v34, v1, s[96:97] offset:2124 sc1
	global_load_dword v35, v1, s[96:97] offset:2128 sc1
	global_load_dword v36, v1, s[96:97] offset:2132 sc1
	global_load_dword v37, v1, s[96:97] offset:2136 sc1
	global_load_dword v38, v1, s[96:97] offset:2140 sc1
	global_load_dword v39, v1, s[96:97] offset:2144 sc1
	global_load_dword v40, v1, s[96:97] offset:2148 sc1
	global_load_dword v41, v1, s[96:97] offset:2152 sc1
	global_load_dword v42, v1, s[96:97] offset:2156 sc1
	global_load_dword v43, v1, s[96:97] offset:2160 sc1
	global_load_dword v44, v1, s[96:97] offset:2164 sc1
	global_load_dword v45, v1, s[96:97] offset:2168 sc1
	global_load_dword v46, v1, s[96:97] offset:2172 sc1
	s_add_i32 s2, 0, 0x27c80
	v_mov_b32_e32 v4, s2
	ds_write_b32 v4, v1
	s_add_i32 s3, 0, 0x27c00
	v_mov_b32_e32 v5, s3
	s_add_i32 s2, 0, 0x27c84
	s_waitcnt vmcnt(15)
	v_mov_b32_e32 v6, s2
	s_add_i32 s3, 0, 0x27c04
	v_mov_b32_e32 v7, s3
	s_add_i32 s2, 0, 0x27c88
	s_add_i32 s3, 0, 0x27c08
	s_waitcnt vmcnt(0)
	v_add_u32_e32 v3, 0xff, v3
	v_ashrrev_i32_e32 v4, 31, v3
	v_add_u32_sdwa v3, v3, v4 dst_sel:DWORD dst_unused:UNUSED_PAD src0_sel:DWORD src1_sel:BYTE_3
	v_and_b32_e32 v4, 0xffffff00, v3
	ds_write_b32 v5, v4
	v_mov_b32_e32 v5, v16
	ds_write_b32 v6, v4
	v_ashrrev_i32_e32 v3, 8, v3
	v_mov_b32_e32 v6, s2
	s_add_i32 s2, 0, 0x27c8c
	s_waitcnt vmcnt(0)
	v_add_u32_e32 v4, 0xff, v5
	v_ashrrev_i32_e32 v5, 31, v4
	v_add_u32_sdwa v4, v4, v5 dst_sel:DWORD dst_unused:UNUSED_PAD src0_sel:DWORD src1_sel:BYTE_3
	v_ashrrev_i32_e32 v4, 8, v4
	v_add_u32_e32 v3, v4, v3
	v_lshlrev_b32_e32 v4, 8, v3
	ds_write_b32 v7, v4
	v_mov_b32_e32 v5, v17
	ds_write_b32 v6, v4
	v_mov_b32_e32 v7, s3
	v_mov_b32_e32 v6, s2
	s_add_i32 s3, 0, 0x27c0c
	s_add_i32 s2, 0, 0x27c90
	s_waitcnt vmcnt(0)
	v_add_u32_e32 v4, 0xff, v5
	v_ashrrev_i32_e32 v5, 31, v4
	v_add_u32_sdwa v4, v4, v5 dst_sel:DWORD dst_unused:UNUSED_PAD src0_sel:DWORD src1_sel:BYTE_3
	v_ashrrev_i32_e32 v4, 8, v4
	v_add_u32_e32 v3, v4, v3
	v_lshlrev_b32_e32 v4, 8, v3
	ds_write_b32 v7, v4
	v_mov_b32_e32 v5, v18
	ds_write_b32 v6, v4
	v_mov_b32_e32 v7, s3
	v_mov_b32_e32 v6, s2
	s_add_i32 s3, 0, 0x27c10
	s_add_i32 s2, 0, 0x27c94
	s_waitcnt vmcnt(0)
	v_add_u32_e32 v4, 0xff, v5
	v_ashrrev_i32_e32 v5, 31, v4
	v_add_u32_sdwa v4, v4, v5 dst_sel:DWORD dst_unused:UNUSED_PAD src0_sel:DWORD src1_sel:BYTE_3
	v_ashrrev_i32_e32 v4, 8, v4
	v_add_u32_e32 v3, v4, v3
	v_lshlrev_b32_e32 v4, 8, v3
	ds_write_b32 v7, v4
	v_mov_b32_e32 v5, v19
	ds_write_b32 v6, v4
	v_mov_b32_e32 v7, s3
	v_mov_b32_e32 v6, s2
	s_add_i32 s3, 0, 0x27c14
	s_add_i32 s2, 0, 0x27c98
	s_waitcnt vmcnt(0)
	v_add_u32_e32 v4, 0xff, v5
	v_ashrrev_i32_e32 v5, 31, v4
	v_add_u32_sdwa v4, v4, v5 dst_sel:DWORD dst_unused:UNUSED_PAD src0_sel:DWORD src1_sel:BYTE_3
	v_ashrrev_i32_e32 v4, 8, v4
	v_add_u32_e32 v3, v4, v3
	v_lshlrev_b32_e32 v4, 8, v3
	ds_write_b32 v7, v4
	v_mov_b32_e32 v5, v20
	ds_write_b32 v6, v4
	v_mov_b32_e32 v7, s3
	v_mov_b32_e32 v6, s2
	s_add_i32 s3, 0, 0x27c18
	s_add_i32 s2, 0, 0x27c9c
	s_waitcnt vmcnt(0)
	v_add_u32_e32 v4, 0xff, v5
	v_ashrrev_i32_e32 v5, 31, v4
	v_add_u32_sdwa v4, v4, v5 dst_sel:DWORD dst_unused:UNUSED_PAD src0_sel:DWORD src1_sel:BYTE_3
	v_ashrrev_i32_e32 v4, 8, v4
	v_add_u32_e32 v3, v4, v3
	v_lshlrev_b32_e32 v4, 8, v3
	ds_write_b32 v7, v4
	v_mov_b32_e32 v5, v21
	ds_write_b32 v6, v4
	v_mov_b32_e32 v7, s3
	v_mov_b32_e32 v6, s2
	s_add_i32 s3, 0, 0x27c1c
	s_add_i32 s2, 0, 0x27ca0
	s_waitcnt vmcnt(0)
	v_add_u32_e32 v4, 0xff, v5
	v_ashrrev_i32_e32 v5, 31, v4
	v_add_u32_sdwa v4, v4, v5 dst_sel:DWORD dst_unused:UNUSED_PAD src0_sel:DWORD src1_sel:BYTE_3
	v_ashrrev_i32_e32 v4, 8, v4
	v_add_u32_e32 v3, v4, v3
	v_lshlrev_b32_e32 v4, 8, v3
	ds_write_b32 v7, v4
	v_mov_b32_e32 v5, v22
	ds_write_b32 v6, v4
	v_mov_b32_e32 v7, s3
	v_mov_b32_e32 v6, s2
	s_add_i32 s3, 0, 0x27c20
	s_add_i32 s2, 0, 0x27ca4
	s_waitcnt vmcnt(0)
	v_add_u32_e32 v4, 0xff, v5
	v_ashrrev_i32_e32 v5, 31, v4
	v_add_u32_sdwa v4, v4, v5 dst_sel:DWORD dst_unused:UNUSED_PAD src0_sel:DWORD src1_sel:BYTE_3
	v_ashrrev_i32_e32 v4, 8, v4
	v_add_u32_e32 v3, v4, v3
	v_lshlrev_b32_e32 v4, 8, v3
	ds_write_b32 v7, v4
	v_mov_b32_e32 v5, v23
	ds_write_b32 v6, v4
	v_mov_b32_e32 v7, s3
	v_mov_b32_e32 v6, s2
	s_add_i32 s3, 0, 0x27c24
	s_add_i32 s2, 0, 0x27ca8
	s_waitcnt vmcnt(0)
; __device__ __forceinline__ void moe_tables(Frame& F) {
;     ...
;         for (int e = 0; e < NE; ++e) { const int c = (int)__hip_atomic_load(F.ctl + CW_CNT + e, RLX_AGENT); const int p = (c + 255) / 256 * 256; tab[32 + e] = run; run += p; tab[e] = run; }
	v_add_u32_e32 v4, 0xff, v5
	v_ashrrev_i32_e32 v5, 31, v4
	v_add_u32_sdwa v4, v4, v5 dst_sel:DWORD dst_unused:UNUSED_PAD src0_sel:DWORD src1_sel:BYTE_3
	v_ashrrev_i32_e32 v4, 8, v4
	v_add_u32_e32 v3, v4, v3
	v_lshlrev_b32_e32 v4, 8, v3
	ds_write_b32 v7, v4
	v_mov_b32_e32 v5, v24
	ds_write_b32 v6, v4
	v_mov_b32_e32 v7, s3
	v_mov_b32_e32 v6, s2
	s_add_i32 s3, 0, 0x27c28
	s_add_i32 s2, 0, 0x27cac
	s_waitcnt vmcnt(0)
	v_add_u32_e32 v4, 0xff, v5
	v_ashrrev_i32_e32 v5, 31, v4
	v_add_u32_sdwa v4, v4, v5 dst_sel:DWORD dst_unused:UNUSED_PAD src0_sel:DWORD src1_sel:BYTE_3
	v_ashrrev_i32_e32 v4, 8, v4
	v_add_u32_e32 v3, v4, v3
	v_lshlrev_b32_e32 v4, 8, v3
	ds_write_b32 v7, v4
	v_mov_b32_e32 v5, v25
	ds_write_b32 v6, v4
	v_mov_b32_e32 v7, s3
	v_mov_b32_e32 v6, s2
	s_add_i32 s3, 0, 0x27c2c
	s_add_i32 s2, 0, 0x27cb0
	s_waitcnt vmcnt(0)
	v_add_u32_e32 v4, 0xff, v5
	v_ashrrev_i32_e32 v5, 31, v4
	v_add_u32_sdwa v4, v4, v5 dst_sel:DWORD dst_unused:UNUSED_PAD src0_sel:DWORD src1_sel:BYTE_3
	v_ashrrev_i32_e32 v4, 8, v4
	v_add_u32_e32 v3, v4, v3
	v_lshlrev_b32_e32 v4, 8, v3
	ds_write_b32 v7, v4
	v_mov_b32_e32 v5, v26
	ds_write_b32 v6, v4
	v_mov_b32_e32 v7, s3
	v_mov_b32_e32 v6, s2
	s_add_i32 s3, 0, 0x27c30
	s_add_i32 s2, 0, 0x27cb4
	s_waitcnt vmcnt(0)
	v_add_u32_e32 v4, 0xff, v5
	v_ashrrev_i32_e32 v5, 31, v4
	v_add_u32_sdwa v4, v4, v5 dst_sel:DWORD dst_unused:UNUSED_PAD src0_sel:DWORD src1_sel:BYTE_3
	v_ashrrev_i32_e32 v4, 8, v4
	v_add_u32_e32 v3, v4, v3
	v_lshlrev_b32_e32 v4, 8, v3
	ds_write_b32 v7, v4
	v_mov_b32_e32 v5, v27
	ds_write_b32 v6, v4
	v_mov_b32_e32 v7, s3
	v_mov_b32_e32 v6, s2
	s_add_i32 s3, 0, 0x27c34
	s_add_i32 s2, 0, 0x27cb8
	s_waitcnt vmcnt(0)
	v_add_u32_e32 v4, 0xff, v5
	v_ashrrev_i32_e32 v5, 31, v4
	v_add_u32_sdwa v4, v4, v5 dst_sel:DWORD dst_unused:UNUSED_PAD src0_sel:DWORD src1_sel:BYTE_3
	v_ashrrev_i32_e32 v4, 8, v4
	v_add_u32_e32 v3, v4, v3
	v_lshlrev_b32_e32 v4, 8, v3
	ds_write_b32 v7, v4
	v_mov_b32_e32 v5, v28
	ds_write_b32 v6, v4
	v_mov_b32_e32 v7, s3
	v_mov_b32_e32 v6, s2
	s_add_i32 s3, 0, 0x27c38
	s_add_i32 s2, 0, 0x27cbc
	s_waitcnt vmcnt(0)
	v_add_u32_e32 v4, 0xff, v5
	v_ashrrev_i32_e32 v5, 31, v4
	v_add_u32_sdwa v4, v4, v5 dst_sel:DWORD dst_unused:UNUSED_PAD src0_sel:DWORD src1_sel:BYTE_3
	v_ashrrev_i32_e32 v4, 8, v4
	v_add_u32_e32 v3, v4, v3
	v_lshlrev_b32_e32 v4, 8, v3
	ds_write_b32 v7, v4
	v_mov_b32_e32 v5, v29
	ds_write_b32 v6, v4
	v_mov_b32_e32 v7, s3
	v_mov_b32_e32 v6, s2
	s_add_i32 s3, 0, 0x27c3c
	s_add_i32 s2, 0, 0x27cc0
	s_waitcnt vmcnt(0)
	v_add_u32_e32 v4, 0xff, v5
	v_ashrrev_i32_e32 v5, 31, v4
	v_add_u32_sdwa v4, v4, v5 dst_sel:DWORD dst_unused:UNUSED_PAD src0_sel:DWORD src1_sel:BYTE_3
	v_ashrrev_i32_e32 v4, 8, v4
	v_add_u32_e32 v3, v4, v3
	v_lshlrev_b32_e32 v4, 8, v3
	ds_write_b32 v7, v4
	v_mov_b32_e32 v5, v30
	ds_write_b32 v6, v4
	v_mov_b32_e32 v7, s3
	v_mov_b32_e32 v6, s2
	s_add_i32 s3, 0, 0x27c40
	s_add_i32 s2, 0, 0x27cc4
	s_waitcnt vmcnt(0)
	v_add_u32_e32 v4, 0xff, v5
	v_ashrrev_i32_e32 v5, 31, v4
	v_add_u32_sdwa v4, v4, v5 dst_sel:DWORD dst_unused:UNUSED_PAD src0_sel:DWORD src1_sel:BYTE_3
	v_ashrrev_i32_e32 v4, 8, v4
	v_add_u32_e32 v3, v4, v3
	v_lshlrev_b32_e32 v4, 8, v3
	ds_write_b32 v7, v4
	v_mov_b32_e32 v5, v31
	ds_write_b32 v6, v4
	v_mov_b32_e32 v7, s3
	v_mov_b32_e32 v6, s2
	s_add_i32 s3, 0, 0x27c44
	s_add_i32 s2, 0, 0x27cc8
	s_waitcnt vmcnt(0)
	v_add_u32_e32 v4, 0xff, v5
	v_ashrrev_i32_e32 v5, 31, v4
	v_add_u32_sdwa v4, v4, v5 dst_sel:DWORD dst_unused:UNUSED_PAD src0_sel:DWORD src1_sel:BYTE_3
	v_ashrrev_i32_e32 v4, 8, v4
	v_add_u32_e32 v3, v4, v3
	v_lshlrev_b32_e32 v4, 8, v3
	ds_write_b32 v7, v4
	v_mov_b32_e32 v5, v32
	ds_write_b32 v6, v4
	v_mov_b32_e32 v7, s3
	v_mov_b32_e32 v6, s2
	s_add_i32 s3, 0, 0x27c48
	s_add_i32 s2, 0, 0x27ccc
	s_waitcnt vmcnt(0)
	v_add_u32_e32 v4, 0xff, v5
	v_ashrrev_i32_e32 v5, 31, v4
	v_add_u32_sdwa v4, v4, v5 dst_sel:DWORD dst_unused:UNUSED_PAD src0_sel:DWORD src1_sel:BYTE_3
	v_ashrrev_i32_e32 v4, 8, v4
	v_add_u32_e32 v3, v4, v3
	v_lshlrev_b32_e32 v4, 8, v3
	ds_write_b32 v7, v4
	v_mov_b32_e32 v5, v33
	ds_write_b32 v6, v4
	v_mov_b32_e32 v7, s3
	v_mov_b32_e32 v6, s2
	s_add_i32 s3, 0, 0x27c4c
	s_add_i32 s2, 0, 0x27cd0
	s_waitcnt vmcnt(0)
	v_add_u32_e32 v4, 0xff, v5
	v_ashrrev_i32_e32 v5, 31, v4
	v_add_u32_sdwa v4, v4, v5 dst_sel:DWORD dst_unused:UNUSED_PAD src0_sel:DWORD src1_sel:BYTE_3
	v_ashrrev_i32_e32 v4, 8, v4
	v_add_u32_e32 v3, v4, v3
	v_lshlrev_b32_e32 v4, 8, v3
	ds_write_b32 v7, v4
	v_mov_b32_e32 v5, v34
	ds_write_b32 v6, v4
	v_mov_b32_e32 v7, s3
	v_mov_b32_e32 v6, s2
	s_add_i32 s3, 0, 0x27c50
	s_add_i32 s2, 0, 0x27cd4
	s_waitcnt vmcnt(0)
	v_add_u32_e32 v4, 0xff, v5
	v_ashrrev_i32_e32 v5, 31, v4
	v_add_u32_sdwa v4, v4, v5 dst_sel:DWORD dst_unused:UNUSED_PAD src0_sel:DWORD src1_sel:BYTE_3
	v_ashrrev_i32_e32 v4, 8, v4
	v_add_u32_e32 v3, v4, v3
	v_lshlrev_b32_e32 v4, 8, v3
	ds_write_b32 v7, v4
	v_mov_b32_e32 v5, v35
	ds_write_b32 v6, v4
	v_mov_b32_e32 v7, s3
	v_mov_b32_e32 v6, s2
	s_add_i32 s3, 0, 0x27c54
	s_add_i32 s2, 0, 0x27cd8
	s_waitcnt vmcnt(0)
; __device__ __forceinline__ void moe_tables(Frame& F) {
;     ...
;         for (int e = 0; e < NE; ++e) { const int c = (int)__hip_atomic_load(F.ctl + CW_CNT + e, RLX_AGENT); const int p = (c + 255) / 256 * 256; tab[32 + e] = run; run += p; tab[e] = run; }
;         tab[64] = run / 256; }
	v_add_u32_e32 v4, 0xff, v5
	v_ashrrev_i32_e32 v5, 31, v4
	v_add_u32_sdwa v4, v4, v5 dst_sel:DWORD dst_unused:UNUSED_PAD src0_sel:DWORD src1_sel:BYTE_3
	v_ashrrev_i32_e32 v4, 8, v4
	v_add_u32_e32 v3, v4, v3
	v_lshlrev_b32_e32 v4, 8, v3
	ds_write_b32 v7, v4
	v_mov_b32_e32 v5, v36
	ds_write_b32 v6, v4
	v_mov_b32_e32 v7, s3
	v_mov_b32_e32 v6, s2
	s_add_i32 s3, 0, 0x27c58
	s_add_i32 s2, 0, 0x27cdc
	s_waitcnt vmcnt(0)
	v_add_u32_e32 v4, 0xff, v5
	v_ashrrev_i32_e32 v5, 31, v4
	v_add_u32_sdwa v4, v4, v5 dst_sel:DWORD dst_unused:UNUSED_PAD src0_sel:DWORD src1_sel:BYTE_3
	v_ashrrev_i32_e32 v4, 8, v4
	v_add_u32_e32 v3, v4, v3
	v_lshlrev_b32_e32 v4, 8, v3
	ds_write_b32 v7, v4
	v_mov_b32_e32 v5, v37
	ds_write_b32 v6, v4
	v_mov_b32_e32 v7, s3
	v_mov_b32_e32 v6, s2
	s_add_i32 s3, 0, 0x27c5c
	s_add_i32 s2, 0, 0x27ce0
	s_waitcnt vmcnt(0)
	v_add_u32_e32 v4, 0xff, v5
	v_ashrrev_i32_e32 v5, 31, v4
	v_add_u32_sdwa v4, v4, v5 dst_sel:DWORD dst_unused:UNUSED_PAD src0_sel:DWORD src1_sel:BYTE_3
	v_ashrrev_i32_e32 v4, 8, v4
	v_add_u32_e32 v3, v4, v3
	v_lshlrev_b32_e32 v4, 8, v3
	ds_write_b32 v7, v4
	v_mov_b32_e32 v5, v38
	ds_write_b32 v6, v4
	v_mov_b32_e32 v7, s3
	v_mov_b32_e32 v6, s2
	s_add_i32 s3, 0, 0x27c60
	s_add_i32 s2, 0, 0x27ce4
	s_waitcnt vmcnt(0)
	v_add_u32_e32 v4, 0xff, v5
	v_ashrrev_i32_e32 v5, 31, v4
	v_add_u32_sdwa v4, v4, v5 dst_sel:DWORD dst_unused:UNUSED_PAD src0_sel:DWORD src1_sel:BYTE_3
	v_ashrrev_i32_e32 v4, 8, v4
	v_add_u32_e32 v3, v4, v3
	v_lshlrev_b32_e32 v4, 8, v3
	ds_write_b32 v7, v4
	v_mov_b32_e32 v5, v39
	ds_write_b32 v6, v4
	v_mov_b32_e32 v7, s3
	v_mov_b32_e32 v6, s2
	s_add_i32 s3, 0, 0x27c64
	s_add_i32 s2, 0, 0x27ce8
	s_waitcnt vmcnt(0)
	v_add_u32_e32 v4, 0xff, v5
	v_ashrrev_i32_e32 v5, 31, v4
	v_add_u32_sdwa v4, v4, v5 dst_sel:DWORD dst_unused:UNUSED_PAD src0_sel:DWORD src1_sel:BYTE_3
	v_ashrrev_i32_e32 v4, 8, v4
	v_add_u32_e32 v3, v4, v3
	v_lshlrev_b32_e32 v4, 8, v3
	ds_write_b32 v7, v4
	v_mov_b32_e32 v5, v40
	ds_write_b32 v6, v4
	v_mov_b32_e32 v7, s3
	v_mov_b32_e32 v6, s2
	s_add_i32 s3, 0, 0x27c68
	s_add_i32 s2, 0, 0x27cec
	s_waitcnt vmcnt(0)
	v_add_u32_e32 v4, 0xff, v5
	v_ashrrev_i32_e32 v5, 31, v4
	v_add_u32_sdwa v4, v4, v5 dst_sel:DWORD dst_unused:UNUSED_PAD src0_sel:DWORD src1_sel:BYTE_3
	v_ashrrev_i32_e32 v4, 8, v4
	v_add_u32_e32 v3, v4, v3
	v_lshlrev_b32_e32 v4, 8, v3
	ds_write_b32 v7, v4
	v_mov_b32_e32 v5, v41
	ds_write_b32 v6, v4
	v_mov_b32_e32 v7, s3
	v_mov_b32_e32 v6, s2
	s_add_i32 s3, 0, 0x27c6c
	s_add_i32 s2, 0, 0x27cf0
	s_waitcnt vmcnt(0)
	v_add_u32_e32 v4, 0xff, v5
	v_ashrrev_i32_e32 v5, 31, v4
	v_add_u32_sdwa v4, v4, v5 dst_sel:DWORD dst_unused:UNUSED_PAD src0_sel:DWORD src1_sel:BYTE_3
	v_ashrrev_i32_e32 v4, 8, v4
	v_add_u32_e32 v3, v4, v3
	v_lshlrev_b32_e32 v4, 8, v3
	ds_write_b32 v7, v4
	v_mov_b32_e32 v5, v42
	ds_write_b32 v6, v4
	v_mov_b32_e32 v7, s3
	v_mov_b32_e32 v6, s2
	s_add_i32 s3, 0, 0x27c70
	s_add_i32 s2, 0, 0x27cf4
	s_waitcnt vmcnt(0)
	v_add_u32_e32 v4, 0xff, v5
	v_ashrrev_i32_e32 v5, 31, v4
	v_add_u32_sdwa v4, v4, v5 dst_sel:DWORD dst_unused:UNUSED_PAD src0_sel:DWORD src1_sel:BYTE_3
	v_ashrrev_i32_e32 v4, 8, v4
	v_add_u32_e32 v3, v4, v3
	v_lshlrev_b32_e32 v4, 8, v3
	ds_write_b32 v7, v4
	v_mov_b32_e32 v5, v43
	ds_write_b32 v6, v4
	v_mov_b32_e32 v7, s3
	v_mov_b32_e32 v6, s2
	s_add_i32 s3, 0, 0x27c74
	s_add_i32 s2, 0, 0x27cf8
	s_waitcnt vmcnt(0)
	v_add_u32_e32 v4, 0xff, v5
	v_ashrrev_i32_e32 v5, 31, v4
	v_add_u32_sdwa v4, v4, v5 dst_sel:DWORD dst_unused:UNUSED_PAD src0_sel:DWORD src1_sel:BYTE_3
	v_ashrrev_i32_e32 v4, 8, v4
	v_add_u32_e32 v3, v4, v3
	v_lshlrev_b32_e32 v4, 8, v3
	ds_write_b32 v7, v4
	v_mov_b32_e32 v5, v44
	ds_write_b32 v6, v4
	v_mov_b32_e32 v7, s3
	v_mov_b32_e32 v6, s2
	s_add_i32 s3, 0, 0x27c78
	s_add_i32 s2, 0, 0x27c7c
	s_waitcnt vmcnt(0)
	v_add_u32_e32 v4, 0xff, v5
	v_ashrrev_i32_e32 v5, 31, v4
	v_add_u32_sdwa v4, v4, v5 dst_sel:DWORD dst_unused:UNUSED_PAD src0_sel:DWORD src1_sel:BYTE_3
	v_ashrrev_i32_e32 v4, 8, v4
	v_add_u32_e32 v3, v4, v3
	v_lshlrev_b32_e32 v4, 8, v3
	ds_write_b32 v7, v4
	v_mov_b32_e32 v5, v45
	ds_write_b32 v6, v4
	v_mov_b32_e32 v7, s3
	s_add_i32 s3, 0, 0x27cfc
	v_mov_b32_e32 v6, s3
	s_waitcnt vmcnt(0)
	v_add_u32_e32 v4, 0xff, v5
	v_ashrrev_i32_e32 v5, 31, v4
	v_add_u32_sdwa v4, v4, v5 dst_sel:DWORD dst_unused:UNUSED_PAD src0_sel:DWORD src1_sel:BYTE_3
	v_ashrrev_i32_e32 v4, 8, v4
	v_add_u32_e32 v3, v4, v3
	v_lshlrev_b32_e32 v4, 8, v3
	ds_write_b32 v7, v4
	v_mov_b32_e32 v1, v46
	v_mov_b32_e32 v5, s2
	s_waitcnt vmcnt(0)
	v_add_u32_e32 v1, 0xff, v1
	v_ashrrev_i32_e32 v7, 31, v1
	v_add_u32_sdwa v1, v1, v7 dst_sel:DWORD dst_unused:UNUSED_PAD src0_sel:DWORD src1_sel:BYTE_3
	v_lshrrev_b32_e32 v1, 8, v1
	v_add_u32_e32 v1, v1, v3
	v_lshlrev_b32_e32 v3, 8, v1
	v_bfe_i32 v1, v1, 0, 24
	ds_write_b32 v5, v3
	ds_write2_b32 v6, v4, v1 offset1:1

; #define LAS __attribute__((address_space(3)))
; __device__ __forceinline__ void moe_tables(Frame& F) {
;     LAS int* tab = (LAS int*)(F.lds + TAB_OFF);
;     if (F.tid == 0) { int run = 0;
;         for (int e = 0; e < NE; ++e) { const int c = (int)__hip_atomic_load(F.ctl + CW_CNT + e, RLX_AGENT); const int p = (c + 255) / 256 * 256; tab[32 + e] = run; run += p; tab[e] = run; }
;         tab[64] = run / 256; }
;     __syncthreads();
; }
.LBB0_1638:
	s_or_b64 exec, exec, s[0:1]
	s_waitcnt lgkmcnt(0)
	v_mov_b32_e32 v1, v0
	s_barrier
	s_nop 0
	v_cmp_eq_u32_e32 vcc, 0, v1
	s_and_saveexec_b64 s[0:1], vcc
	s_cbranch_execz .LBB0_1640
	v_mov_b32_e32 v1, 0
	global_load_dword v2, v1, s[96:97] offset:2048 sc1
	global_load_dword v16, v1, s[96:97] offset:2052 sc1
	global_load_dword v17, v1, s[96:97] offset:2056 sc1
	global_load_dword v18, v1, s[96:97] offset:2060 sc1
	global_load_dword v19, v1, s[96:97] offset:2064 sc1
	global_load_dword v20, v1, s[96:97] offset:2068 sc1
	global_load_dword v21, v1, s[96:97] offset:2072 sc1
	global_load_dword v22, v1, s[96:97] offset:2076 sc1
	global_load_dword v23, v1, s[96:97] offset:2080 sc1
	global_load_dword v24, v1, s[96:97] offset:2084 sc1
	global_load_dword v25, v1, s[96:97] offset:2088 sc1
	global_load_dword v26, v1, s[96:97] offset:2092 sc1
	global_load_dword v27, v1, s[96:97] offset:2096 sc1
	global_load_dword v28, v1, s[96:97] offset:2100 sc1
	global_load_dword v29, v1, s[96:97] offset:2104 sc1
	global_load_dword v30, v1, s[96:97] offset:2108 sc1
	global_load_dword v31, v1, s[96:97] offset:2112 sc1
	global_load_dword v32, v1, s[96:97] offset:2116 sc1
	global_load_dword v33, v1, s[96:97] offset:2120 sc1
	global_load_dword v34, v1, s[96:97] offset:2124 sc1
	global_load_dword v35, v1, s[96:97] offset:2128 sc1
	global_load_dword v36, v1, s[96:97] offset:2132 sc1
	global_load_dword v37, v1, s[96:97] offset:2136 sc1
	global_load_dword v38, v1, s[96:97] offset:2140 sc1
	global_load_dword v39, v1, s[96:97] offset:2144 sc1
	global_load_dword v40, v1, s[96:97] offset:2148 sc1
	global_load_dword v41, v1, s[96:97] offset:2152 sc1
	global_load_dword v42, v1, s[96:97] offset:2156 sc1
	global_load_dword v43, v1, s[96:97] offset:2160 sc1
	global_load_dword v44, v1, s[96:97] offset:2164 sc1
	global_load_dword v45, v1, s[96:97] offset:2168 sc1
	global_load_dword v46, v1, s[96:97] offset:2172 sc1
	s_add_i32 s2, 0, 0x27c80
	v_mov_b32_e32 v3, s2
	ds_write_b32 v3, v1
	s_add_i32 s3, 0, 0x27c00
	v_mov_b32_e32 v4, s3
	s_add_i32 s2, 0, 0x27c84
	v_mov_b32_e32 v5, s2
	s_add_i32 s3, 0, 0x27c04
	s_waitcnt vmcnt(15)
	v_mov_b32_e32 v6, s3
	s_add_i32 s2, 0, 0x27c88
	s_add_i32 s3, 0, 0x27c08
	s_waitcnt vmcnt(0)
	v_add_u32_e32 v2, 0xff, v2
	v_ashrrev_i32_e32 v3, 31, v2
	v_add_u32_sdwa v2, v2, v3 dst_sel:DWORD dst_unused:UNUSED_PAD src0_sel:DWORD src1_sel:BYTE_3
	v_and_b32_e32 v3, 0xffffff00, v2
	ds_write_b32 v4, v3
	v_mov_b32_e32 v4, v16
	ds_write_b32 v5, v3
	v_ashrrev_i32_e32 v2, 8, v2
	v_mov_b32_e32 v5, s2
	s_add_i32 s2, 0, 0x27c8c
	s_waitcnt vmcnt(0)
	v_add_u32_e32 v3, 0xff, v4
	v_ashrrev_i32_e32 v4, 31, v3
	v_add_u32_sdwa v3, v3, v4 dst_sel:DWORD dst_unused:UNUSED_PAD src0_sel:DWORD src1_sel:BYTE_3
	v_ashrrev_i32_e32 v3, 8, v3
	v_add_u32_e32 v2, v3, v2
	v_lshlrev_b32_e32 v3, 8, v2
	ds_write_b32 v6, v3
	v_mov_b32_e32 v4, v17
	ds_write_b32 v5, v3
	v_mov_b32_e32 v6, s3
	v_mov_b32_e32 v5, s2
	s_add_i32 s3, 0, 0x27c0c
	s_add_i32 s2, 0, 0x27c90
	s_waitcnt vmcnt(0)
	v_add_u32_e32 v3, 0xff, v4
	v_ashrrev_i32_e32 v4, 31, v3
	v_add_u32_sdwa v3, v3, v4 dst_sel:DWORD dst_unused:UNUSED_PAD src0_sel:DWORD src1_sel:BYTE_3
	v_ashrrev_i32_e32 v3, 8, v3
	v_add_u32_e32 v2, v3, v2
	v_lshlrev_b32_e32 v3, 8, v2
	ds_write_b32 v6, v3
	v_mov_b32_e32 v4, v18
	ds_write_b32 v5, v3
	v_mov_b32_e32 v6, s3
	v_mov_b32_e32 v5, s2
	s_add_i32 s3, 0, 0x27c10
	s_add_i32 s2, 0, 0x27c94
	s_waitcnt vmcnt(0)
	v_add_u32_e32 v3, 0xff, v4
	v_ashrrev_i32_e32 v4, 31, v3
	v_add_u32_sdwa v3, v3, v4 dst_sel:DWORD dst_unused:UNUSED_PAD src0_sel:DWORD src1_sel:BYTE_3
	v_ashrrev_i32_e32 v3, 8, v3
	v_add_u32_e32 v2, v3, v2
	v_lshlrev_b32_e32 v3, 8, v2
	ds_write_b32 v6, v3
	v_mov_b32_e32 v4, v19
	ds_write_b32 v5, v3
	v_mov_b32_e32 v6, s3
	v_mov_b32_e32 v5, s2
	s_add_i32 s3, 0, 0x27c14
	s_add_i32 s2, 0, 0x27c98
	s_waitcnt vmcnt(0)
	v_add_u32_e32 v3, 0xff, v4
	v_ashrrev_i32_e32 v4, 31, v3
	v_add_u32_sdwa v3, v3, v4 dst_sel:DWORD dst_unused:UNUSED_PAD src0_sel:DWORD src1_sel:BYTE_3
	v_ashrrev_i32_e32 v3, 8, v3
	v_add_u32_e32 v2, v3, v2
	v_lshlrev_b32_e32 v3, 8, v2
	ds_write_b32 v6, v3
	v_mov_b32_e32 v4, v20
	ds_write_b32 v5, v3
	v_mov_b32_e32 v6, s3
	v_mov_b32_e32 v5, s2
	s_add_i32 s3, 0, 0x27c18
	s_add_i32 s2, 0, 0x27c9c
	s_waitcnt vmcnt(0)
	v_add_u32_e32 v3, 0xff, v4
	v_ashrrev_i32_e32 v4, 31, v3
	v_add_u32_sdwa v3, v3, v4 dst_sel:DWORD dst_unused:UNUSED_PAD src0_sel:DWORD src1_sel:BYTE_3
	v_ashrrev_i32_e32 v3, 8, v3
	v_add_u32_e32 v2, v3, v2
	v_lshlrev_b32_e32 v3, 8, v2
	ds_write_b32 v6, v3
	v_mov_b32_e32 v4, v21
	ds_write_b32 v5, v3
	v_mov_b32_e32 v6, s3
	v_mov_b32_e32 v5, s2
	s_add_i32 s3, 0, 0x27c1c
	s_add_i32 s2, 0, 0x27ca0
	s_waitcnt vmcnt(0)
	v_add_u32_e32 v3, 0xff, v4
	v_ashrrev_i32_e32 v4, 31, v3
	v_add_u32_sdwa v3, v3, v4 dst_sel:DWORD dst_unused:UNUSED_PAD src0_sel:DWORD src1_sel:BYTE_3
	v_ashrrev_i32_e32 v3, 8, v3
	v_add_u32_e32 v2, v3, v2
	v_lshlrev_b32_e32 v3, 8, v2
	ds_write_b32 v6, v3
	v_mov_b32_e32 v4, v22
	ds_write_b32 v5, v3
	v_mov_b32_e32 v6, s3
	v_mov_b32_e32 v5, s2
	s_add_i32 s3, 0, 0x27c20
	s_add_i32 s2, 0, 0x27ca4
	s_waitcnt vmcnt(0)
	v_add_u32_e32 v3, 0xff, v4
	v_ashrrev_i32_e32 v4, 31, v3
	v_add_u32_sdwa v3, v3, v4 dst_sel:DWORD dst_unused:UNUSED_PAD src0_sel:DWORD src1_sel:BYTE_3
	v_ashrrev_i32_e32 v3, 8, v3
	v_add_u32_e32 v2, v3, v2
	v_lshlrev_b32_e32 v3, 8, v2
	ds_write_b32 v6, v3
	v_mov_b32_e32 v4, v23
	ds_write_b32 v5, v3
	v_mov_b32_e32 v6, s3
	v_mov_b32_e32 v5, s2
	s_add_i32 s3, 0, 0x27c24
	s_add_i32 s2, 0, 0x27ca8
	s_waitcnt vmcnt(0)
; __device__ __forceinline__ void moe_tables(Frame& F) {
;     ...
;         for (int e = 0; e < NE; ++e) { const int c = (int)__hip_atomic_load(F.ctl + CW_CNT + e, RLX_AGENT); const int p = (c + 255) / 256 * 256; tab[32 + e] = run; run += p; tab[e] = run; }
	v_add_u32_e32 v3, 0xff, v4
	v_ashrrev_i32_e32 v4, 31, v3
	v_add_u32_sdwa v3, v3, v4 dst_sel:DWORD dst_unused:UNUSED_PAD src0_sel:DWORD src1_sel:BYTE_3
	v_ashrrev_i32_e32 v3, 8, v3
	v_add_u32_e32 v2, v3, v2
	v_lshlrev_b32_e32 v3, 8, v2
	ds_write_b32 v6, v3
	v_mov_b32_e32 v4, v24
	ds_write_b32 v5, v3
	v_mov_b32_e32 v6, s3
	v_mov_b32_e32 v5, s2
	s_add_i32 s3, 0, 0x27c28
	s_add_i32 s2, 0, 0x27cac
	s_waitcnt vmcnt(0)
	v_add_u32_e32 v3, 0xff, v4
	v_ashrrev_i32_e32 v4, 31, v3
	v_add_u32_sdwa v3, v3, v4 dst_sel:DWORD dst_unused:UNUSED_PAD src0_sel:DWORD src1_sel:BYTE_3
	v_ashrrev_i32_e32 v3, 8, v3
	v_add_u32_e32 v2, v3, v2
	v_lshlrev_b32_e32 v3, 8, v2
	ds_write_b32 v6, v3
	v_mov_b32_e32 v4, v25
	ds_write_b32 v5, v3
	v_mov_b32_e32 v6, s3
	v_mov_b32_e32 v5, s2
	s_add_i32 s3, 0, 0x27c2c
	s_add_i32 s2, 0, 0x27cb0
	s_waitcnt vmcnt(0)
	v_add_u32_e32 v3, 0xff, v4
	v_ashrrev_i32_e32 v4, 31, v3
	v_add_u32_sdwa v3, v3, v4 dst_sel:DWORD dst_unused:UNUSED_PAD src0_sel:DWORD src1_sel:BYTE_3
	v_ashrrev_i32_e32 v3, 8, v3
	v_add_u32_e32 v2, v3, v2
	v_lshlrev_b32_e32 v3, 8, v2
	ds_write_b32 v6, v3
	v_mov_b32_e32 v4, v26
	ds_write_b32 v5, v3
	v_mov_b32_e32 v6, s3
	v_mov_b32_e32 v5, s2
	s_add_i32 s3, 0, 0x27c30
	s_add_i32 s2, 0, 0x27cb4
	s_waitcnt vmcnt(0)
	v_add_u32_e32 v3, 0xff, v4
	v_ashrrev_i32_e32 v4, 31, v3
	v_add_u32_sdwa v3, v3, v4 dst_sel:DWORD dst_unused:UNUSED_PAD src0_sel:DWORD src1_sel:BYTE_3
	v_ashrrev_i32_e32 v3, 8, v3
	v_add_u32_e32 v2, v3, v2
	v_lshlrev_b32_e32 v3, 8, v2
	ds_write_b32 v6, v3
	v_mov_b32_e32 v4, v27
	ds_write_b32 v5, v3
	v_mov_b32_e32 v6, s3
	v_mov_b32_e32 v5, s2
	s_add_i32 s3, 0, 0x27c34
	s_add_i32 s2, 0, 0x27cb8
	s_waitcnt vmcnt(0)
	v_add_u32_e32 v3, 0xff, v4
	v_ashrrev_i32_e32 v4, 31, v3
	v_add_u32_sdwa v3, v3, v4 dst_sel:DWORD dst_unused:UNUSED_PAD src0_sel:DWORD src1_sel:BYTE_3
	v_ashrrev_i32_e32 v3, 8, v3
	v_add_u32_e32 v2, v3, v2
	v_lshlrev_b32_e32 v3, 8, v2
	ds_write_b32 v6, v3
	v_mov_b32_e32 v4, v28
	ds_write_b32 v5, v3
	v_mov_b32_e32 v6, s3
	v_mov_b32_e32 v5, s2
	s_add_i32 s3, 0, 0x27c38
	s_add_i32 s2, 0, 0x27cbc
	s_waitcnt vmcnt(0)
	v_add_u32_e32 v3, 0xff, v4
	v_ashrrev_i32_e32 v4, 31, v3
	v_add_u32_sdwa v3, v3, v4 dst_sel:DWORD dst_unused:UNUSED_PAD src0_sel:DWORD src1_sel:BYTE_3
	v_ashrrev_i32_e32 v3, 8, v3
	v_add_u32_e32 v2, v3, v2
	v_lshlrev_b32_e32 v3, 8, v2
	ds_write_b32 v6, v3
	v_mov_b32_e32 v4, v29
	ds_write_b32 v5, v3
	v_mov_b32_e32 v6, s3
	v_mov_b32_e32 v5, s2
	s_add_i32 s3, 0, 0x27c3c
	s_add_i32 s2, 0, 0x27cc0
	s_waitcnt vmcnt(0)
	v_add_u32_e32 v3, 0xff, v4
	v_ashrrev_i32_e32 v4, 31, v3
	v_add_u32_sdwa v3, v3, v4 dst_sel:DWORD dst_unused:UNUSED_PAD src0_sel:DWORD src1_sel:BYTE_3
	v_ashrrev_i32_e32 v3, 8, v3
	v_add_u32_e32 v2, v3, v2
	v_lshlrev_b32_e32 v3, 8, v2
	ds_write_b32 v6, v3
	v_mov_b32_e32 v4, v30
	ds_write_b32 v5, v3
	v_mov_b32_e32 v6, s3
	v_mov_b32_e32 v5, s2
	s_add_i32 s3, 0, 0x27c40
	s_add_i32 s2, 0, 0x27cc4
	s_waitcnt vmcnt(0)
	v_add_u32_e32 v3, 0xff, v4
	v_ashrrev_i32_e32 v4, 31, v3
	v_add_u32_sdwa v3, v3, v4 dst_sel:DWORD dst_unused:UNUSED_PAD src0_sel:DWORD src1_sel:BYTE_3
	v_ashrrev_i32_e32 v3, 8, v3
	v_add_u32_e32 v2, v3, v2
	v_lshlrev_b32_e32 v3, 8, v2
	ds_write_b32 v6, v3
	v_mov_b32_e32 v4, v31
	ds_write_b32 v5, v3
	v_mov_b32_e32 v6, s3
	v_mov_b32_e32 v5, s2
	s_add_i32 s3, 0, 0x27c44
	s_add_i32 s2, 0, 0x27cc8
	s_waitcnt vmcnt(0)
	v_add_u32_e32 v3, 0xff, v4
	v_ashrrev_i32_e32 v4, 31, v3
	v_add_u32_sdwa v3, v3, v4 dst_sel:DWORD dst_unused:UNUSED_PAD src0_sel:DWORD src1_sel:BYTE_3
	v_ashrrev_i32_e32 v3, 8, v3
	v_add_u32_e32 v2, v3, v2
	v_lshlrev_b32_e32 v3, 8, v2
	ds_write_b32 v6, v3
	v_mov_b32_e32 v4, v32
	ds_write_b32 v5, v3
	v_mov_b32_e32 v6, s3
	v_mov_b32_e32 v5, s2
	s_add_i32 s3, 0, 0x27c48
	s_add_i32 s2, 0, 0x27ccc
	s_waitcnt vmcnt(0)
	v_add_u32_e32 v3, 0xff, v4
	v_ashrrev_i32_e32 v4, 31, v3
	v_add_u32_sdwa v3, v3, v4 dst_sel:DWORD dst_unused:UNUSED_PAD src0_sel:DWORD src1_sel:BYTE_3
	v_ashrrev_i32_e32 v3, 8, v3
	v_add_u32_e32 v2, v3, v2
	v_lshlrev_b32_e32 v3, 8, v2
	ds_write_b32 v6, v3
	v_mov_b32_e32 v4, v33
	ds_write_b32 v5, v3
	v_mov_b32_e32 v6, s3
	v_mov_b32_e32 v5, s2
	s_add_i32 s3, 0, 0x27c4c
	s_add_i32 s2, 0, 0x27cd0
	s_waitcnt vmcnt(0)
	v_add_u32_e32 v3, 0xff, v4
	v_ashrrev_i32_e32 v4, 31, v3
	v_add_u32_sdwa v3, v3, v4 dst_sel:DWORD dst_unused:UNUSED_PAD src0_sel:DWORD src1_sel:BYTE_3
	v_ashrrev_i32_e32 v3, 8, v3
	v_add_u32_e32 v2, v3, v2
	v_lshlrev_b32_e32 v3, 8, v2
	ds_write_b32 v6, v3
	v_mov_b32_e32 v4, v34
	ds_write_b32 v5, v3
	v_mov_b32_e32 v6, s3
	v_mov_b32_e32 v5, s2
	s_add_i32 s3, 0, 0x27c50
	s_add_i32 s2, 0, 0x27cd4
	s_waitcnt vmcnt(0)
	v_add_u32_e32 v3, 0xff, v4
	v_ashrrev_i32_e32 v4, 31, v3
	v_add_u32_sdwa v3, v3, v4 dst_sel:DWORD dst_unused:UNUSED_PAD src0_sel:DWORD src1_sel:BYTE_3
	v_ashrrev_i32_e32 v3, 8, v3
	v_add_u32_e32 v2, v3, v2
	v_lshlrev_b32_e32 v3, 8, v2
	ds_write_b32 v6, v3
	v_mov_b32_e32 v4, v35
	ds_write_b32 v5, v3
	v_mov_b32_e32 v6, s3
	v_mov_b32_e32 v5, s2
	s_add_i32 s3, 0, 0x27c54
	s_add_i32 s2, 0, 0x27cd8
	s_waitcnt vmcnt(0)
; __device__ __forceinline__ void moe_tables(Frame& F) {
;     ...
;         for (int e = 0; e < NE; ++e) { const int c = (int)__hip_atomic_load(F.ctl + CW_CNT + e, RLX_AGENT); const int p = (c + 255) / 256 * 256; tab[32 + e] = run; run += p; tab[e] = run; }
;         tab[64] = run / 256; }
	v_add_u32_e32 v3, 0xff, v4
	v_ashrrev_i32_e32 v4, 31, v3
	v_add_u32_sdwa v3, v3, v4 dst_sel:DWORD dst_unused:UNUSED_PAD src0_sel:DWORD src1_sel:BYTE_3
	v_ashrrev_i32_e32 v3, 8, v3
	v_add_u32_e32 v2, v3, v2
	v_lshlrev_b32_e32 v3, 8, v2
	ds_write_b32 v6, v3
	v_mov_b32_e32 v4, v36
	ds_write_b32 v5, v3
	v_mov_b32_e32 v6, s3
	v_mov_b32_e32 v5, s2
	s_add_i32 s3, 0, 0x27c58
	s_add_i32 s2, 0, 0x27cdc
	s_waitcnt vmcnt(0)
	v_add_u32_e32 v3, 0xff, v4
	v_ashrrev_i32_e32 v4, 31, v3
	v_add_u32_sdwa v3, v3, v4 dst_sel:DWORD dst_unused:UNUSED_PAD src0_sel:DWORD src1_sel:BYTE_3
	v_ashrrev_i32_e32 v3, 8, v3
	v_add_u32_e32 v2, v3, v2
	v_lshlrev_b32_e32 v3, 8, v2
	ds_write_b32 v6, v3
	v_mov_b32_e32 v4, v37
	ds_write_b32 v5, v3
	v_mov_b32_e32 v6, s3
	v_mov_b32_e32 v5, s2
	s_add_i32 s3, 0, 0x27c5c
	s_add_i32 s2, 0, 0x27ce0
	s_waitcnt vmcnt(0)
	v_add_u32_e32 v3, 0xff, v4
	v_ashrrev_i32_e32 v4, 31, v3
	v_add_u32_sdwa v3, v3, v4 dst_sel:DWORD dst_unused:UNUSED_PAD src0_sel:DWORD src1_sel:BYTE_3
	v_ashrrev_i32_e32 v3, 8, v3
	v_add_u32_e32 v2, v3, v2
	v_lshlrev_b32_e32 v3, 8, v2
	ds_write_b32 v6, v3
	v_mov_b32_e32 v4, v38
	ds_write_b32 v5, v3
	v_mov_b32_e32 v6, s3
	v_mov_b32_e32 v5, s2
	s_add_i32 s3, 0, 0x27c60
	s_add_i32 s2, 0, 0x27ce4
	s_waitcnt vmcnt(0)
	v_add_u32_e32 v3, 0xff, v4
	v_ashrrev_i32_e32 v4, 31, v3
	v_add_u32_sdwa v3, v3, v4 dst_sel:DWORD dst_unused:UNUSED_PAD src0_sel:DWORD src1_sel:BYTE_3
	v_ashrrev_i32_e32 v3, 8, v3
	v_add_u32_e32 v2, v3, v2
	v_lshlrev_b32_e32 v3, 8, v2
	ds_write_b32 v6, v3
	v_mov_b32_e32 v4, v39
	ds_write_b32 v5, v3
	v_mov_b32_e32 v6, s3
	v_mov_b32_e32 v5, s2
	s_add_i32 s3, 0, 0x27c64
	s_add_i32 s2, 0, 0x27ce8
	s_waitcnt vmcnt(0)
	v_add_u32_e32 v3, 0xff, v4
	v_ashrrev_i32_e32 v4, 31, v3
	v_add_u32_sdwa v3, v3, v4 dst_sel:DWORD dst_unused:UNUSED_PAD src0_sel:DWORD src1_sel:BYTE_3
	v_ashrrev_i32_e32 v3, 8, v3
	v_add_u32_e32 v2, v3, v2
	v_lshlrev_b32_e32 v3, 8, v2
	ds_write_b32 v6, v3
	v_mov_b32_e32 v4, v40
	ds_write_b32 v5, v3
	v_mov_b32_e32 v6, s3
	v_mov_b32_e32 v5, s2
	s_add_i32 s3, 0, 0x27c68
	s_add_i32 s2, 0, 0x27cec
	s_waitcnt vmcnt(0)
	v_add_u32_e32 v3, 0xff, v4
	v_ashrrev_i32_e32 v4, 31, v3
	v_add_u32_sdwa v3, v3, v4 dst_sel:DWORD dst_unused:UNUSED_PAD src0_sel:DWORD src1_sel:BYTE_3
	v_ashrrev_i32_e32 v3, 8, v3
	v_add_u32_e32 v2, v3, v2
	v_lshlrev_b32_e32 v3, 8, v2
	ds_write_b32 v6, v3
	v_mov_b32_e32 v4, v41
	ds_write_b32 v5, v3
	v_mov_b32_e32 v6, s3
	v_mov_b32_e32 v5, s2
	s_add_i32 s3, 0, 0x27c6c
	s_add_i32 s2, 0, 0x27cf0
	s_waitcnt vmcnt(0)
	v_add_u32_e32 v3, 0xff, v4
	v_ashrrev_i32_e32 v4, 31, v3
	v_add_u32_sdwa v3, v3, v4 dst_sel:DWORD dst_unused:UNUSED_PAD src0_sel:DWORD src1_sel:BYTE_3
	v_ashrrev_i32_e32 v3, 8, v3
	v_add_u32_e32 v2, v3, v2
	v_lshlrev_b32_e32 v3, 8, v2
	ds_write_b32 v6, v3
	v_mov_b32_e32 v4, v42
	ds_write_b32 v5, v3
	v_mov_b32_e32 v6, s3
	v_mov_b32_e32 v5, s2
	s_add_i32 s3, 0, 0x27c70
	s_add_i32 s2, 0, 0x27cf4
	s_waitcnt vmcnt(0)
	v_add_u32_e32 v3, 0xff, v4
	v_ashrrev_i32_e32 v4, 31, v3
	v_add_u32_sdwa v3, v3, v4 dst_sel:DWORD dst_unused:UNUSED_PAD src0_sel:DWORD src1_sel:BYTE_3
	v_ashrrev_i32_e32 v3, 8, v3
	v_add_u32_e32 v2, v3, v2
	v_lshlrev_b32_e32 v3, 8, v2
	ds_write_b32 v6, v3
	v_mov_b32_e32 v4, v43
	ds_write_b32 v5, v3
	v_mov_b32_e32 v6, s3
	v_mov_b32_e32 v5, s2
	s_add_i32 s3, 0, 0x27c74
	s_add_i32 s2, 0, 0x27cf8
	s_waitcnt vmcnt(0)
	v_add_u32_e32 v3, 0xff, v4
	v_ashrrev_i32_e32 v4, 31, v3
	v_add_u32_sdwa v3, v3, v4 dst_sel:DWORD dst_unused:UNUSED_PAD src0_sel:DWORD src1_sel:BYTE_3
	v_ashrrev_i32_e32 v3, 8, v3
	v_add_u32_e32 v2, v3, v2
	v_lshlrev_b32_e32 v3, 8, v2
	ds_write_b32 v6, v3
	v_mov_b32_e32 v4, v44
	ds_write_b32 v5, v3
	v_mov_b32_e32 v6, s3
	v_mov_b32_e32 v5, s2
	s_add_i32 s3, 0, 0x27c78
	s_add_i32 s2, 0, 0x27c7c
	s_waitcnt vmcnt(0)
	v_add_u32_e32 v3, 0xff, v4
	v_ashrrev_i32_e32 v4, 31, v3
	v_add_u32_sdwa v3, v3, v4 dst_sel:DWORD dst_unused:UNUSED_PAD src0_sel:DWORD src1_sel:BYTE_3
	v_ashrrev_i32_e32 v3, 8, v3
	v_add_u32_e32 v2, v3, v2
	v_lshlrev_b32_e32 v3, 8, v2
	ds_write_b32 v6, v3
	v_mov_b32_e32 v4, v45
	ds_write_b32 v5, v3
	v_mov_b32_e32 v6, s3
	s_add_i32 s3, 0, 0x27cfc
	v_mov_b32_e32 v5, s3
	s_waitcnt vmcnt(0)
	v_add_u32_e32 v3, 0xff, v4
	v_ashrrev_i32_e32 v4, 31, v3
	v_add_u32_sdwa v3, v3, v4 dst_sel:DWORD dst_unused:UNUSED_PAD src0_sel:DWORD src1_sel:BYTE_3
	v_ashrrev_i32_e32 v3, 8, v3
	v_add_u32_e32 v2, v3, v2
	v_lshlrev_b32_e32 v3, 8, v2
	ds_write_b32 v6, v3
	v_mov_b32_e32 v1, v46
	v_mov_b32_e32 v4, s2
	s_waitcnt vmcnt(0)
	v_add_u32_e32 v1, 0xff, v1
	v_ashrrev_i32_e32 v6, 31, v1
	v_add_u32_sdwa v1, v1, v6 dst_sel:DWORD dst_unused:UNUSED_PAD src0_sel:DWORD src1_sel:BYTE_3
	v_lshrrev_b32_e32 v1, 8, v1
	v_add_u32_e32 v1, v1, v2
	v_lshlrev_b32_e32 v2, 8, v1
	v_bfe_i32 v1, v1, 0, 24
	ds_write_b32 v4, v2
	ds_write2_b32 v5, v3, v1 offset1:1
